# grid barrier: arrive atomic issued before the L1 invalidate, wait vmcnt(1) for the atomic only
# speedup vs baseline: 1.0061x; 1.0061x over previous
.LBB0_188:
	s_mov_b64 s[4:5], exec
	v_readlane_b32 s2, v254, 38
	s_lshl_b32 s2, s2, 8
	v_mbcnt_lo_u32_b32 v1, s4, 0
	s_add_u32 s2, s72, s2
	v_mbcnt_hi_u32_b32 v1, s5, v1
	s_addc_u32 s3, s73, 0
	v_cmp_eq_u32_e32 vcc, 0, v1
	s_and_saveexec_b64 s[6:7], vcc
	s_cbranch_execz .LBB0_190
	s_bcnt1_i32_b64 s4, s[4:5]
	v_mov_b32_e32 v3, 0x1000
	v_mov_b32_e32 v4, s4
	global_atomic_add v3, v3, v4, s[2:3] offset:1024 sc0
	buffer_inv sc1
.LBB0_190:
	s_or_b64 exec, exec, s[6:7]
	v_cvt_f32_u32_e32 v4, v2
	s_waitcnt vmcnt(1)
	v_readfirstlane_b32 s4, v3
	v_sub_u32_e32 v3, 0, v2
	v_rcp_iflag_f32_e32 v4, v4
	v_add_u32_e32 v5, s4, v1
	v_mul_f32_e32 v4, 0x4f7ffffe, v4
	v_cvt_u32_f32_e32 v4, v4
	v_mul_lo_u32 v1, v3, v4
	v_mul_hi_u32 v1, v4, v1
	v_add_u32_e32 v1, v4, v1
	v_mul_hi_u32 v1, v5, v1
	v_mul_lo_u32 v3, v1, v2
	v_sub_u32_e32 v3, v5, v3
	v_add_u32_e32 v4, 1, v1
	v_cmp_ge_u32_e32 vcc, v3, v2
	s_nop 1
	v_cndmask_b32_e32 v1, v1, v4, vcc
	v_sub_u32_e32 v4, v3, v2
	v_cndmask_b32_e32 v3, v3, v4, vcc
	v_add_u32_e32 v4, 1, v1
	v_cmp_ge_u32_e32 vcc, v3, v2
	v_add_u32_e32 v3, 1, v5
	s_nop 0
	v_cndmask_b32_e32 v1, v1, v4, vcc
	v_mul_lo_u32 v4, v2, v1
	v_add_u32_e32 v2, v4, v2
	v_cmp_ne_u32_e32 vcc, v3, v2
	s_and_saveexec_b64 s[4:5], vcc
	s_xor_b64 s[4:5], exec, s[4:5]
	s_cbranch_execz .LBB0_204
	s_waitcnt lgkmcnt(0)
	v_mov_b32_e32 v0, 0x2000
	global_load_dword v0, v0, s[2:3] offset:1024 sc1
	s_add_u32 s8, s2, 0x2400
	s_addc_u32 s9, s3, 0
	s_waitcnt vmcnt(0)
	v_cmp_eq_u32_e32 vcc, v0, v1
	s_and_saveexec_b64 s[6:7], vcc
	s_cbranch_execz .LBB0_203
	s_mov_b32 s16, 1
	s_mov_b64 s[10:11], 0
	v_mov_b32_e32 v0, 0
	s_branch .LBB0_194

.LBB0_264:
	s_mov_b64 s[6:7], exec
	v_readlane_b32 s2, v254, 38
	s_lshl_b32 s2, s2, 8
	v_mbcnt_lo_u32_b32 v1, s6, 0
	s_add_u32 s2, s72, s2
	v_mbcnt_hi_u32_b32 v1, s7, v1
	s_addc_u32 s3, s73, 0
	v_cmp_eq_u32_e32 vcc, 0, v1
	s_and_saveexec_b64 s[8:9], vcc
	s_cbranch_execz .LBB0_266
	s_bcnt1_i32_b64 s6, s[6:7]
	v_mov_b32_e32 v3, 0x1000
	v_mov_b32_e32 v4, s6
	global_atomic_add v3, v3, v4, s[2:3] offset:1024 sc0
	buffer_inv sc1
.LBB0_266:
	s_or_b64 exec, exec, s[8:9]
	v_cvt_f32_u32_e32 v4, v2
	s_waitcnt vmcnt(1)
	v_readfirstlane_b32 s6, v3
	v_sub_u32_e32 v3, 0, v2
	v_rcp_iflag_f32_e32 v4, v4
	v_add_u32_e32 v5, s6, v1
	v_mul_f32_e32 v4, 0x4f7ffffe, v4
	v_cvt_u32_f32_e32 v4, v4
	v_mul_lo_u32 v1, v3, v4
	v_mul_hi_u32 v1, v4, v1
	v_add_u32_e32 v1, v4, v1
	v_mul_hi_u32 v1, v5, v1
	v_mul_lo_u32 v3, v1, v2
	v_sub_u32_e32 v3, v5, v3
	v_add_u32_e32 v4, 1, v1
	v_cmp_ge_u32_e32 vcc, v3, v2
	s_nop 1
	v_cndmask_b32_e32 v1, v1, v4, vcc
	v_sub_u32_e32 v4, v3, v2
	v_cndmask_b32_e32 v3, v3, v4, vcc
	v_add_u32_e32 v4, 1, v1
	v_cmp_ge_u32_e32 vcc, v3, v2
	v_add_u32_e32 v3, 1, v5
	s_nop 0
	v_cndmask_b32_e32 v1, v1, v4, vcc
	v_mul_lo_u32 v4, v2, v1
	v_add_u32_e32 v2, v4, v2
	v_cmp_ne_u32_e32 vcc, v3, v2
	s_and_saveexec_b64 s[6:7], vcc
	s_xor_b64 s[6:7], exec, s[6:7]
	s_cbranch_execz .LBB0_280
	s_waitcnt lgkmcnt(0)
	v_mov_b32_e32 v0, 0x2000
	global_load_dword v0, v0, s[2:3] offset:1024 sc1
	s_add_u32 s10, s2, 0x2400
	s_addc_u32 s11, s3, 0
	s_waitcnt vmcnt(0)
	v_cmp_eq_u32_e32 vcc, v0, v1
	s_and_saveexec_b64 s[8:9], vcc
	s_cbranch_execz .LBB0_279
	s_mov_b32 s16, 1
	s_mov_b64 s[12:13], 0
	v_mov_b32_e32 v0, 0
	s_branch .LBB0_270

.LBB0_690:
	s_or_b64 exec, exec, s[6:7]
	v_cvt_f32_u32_e32 v4, v2
	s_waitcnt vmcnt(1)
	v_readfirstlane_b32 s4, v3
	v_sub_u32_e32 v3, 0, v2
	v_rcp_iflag_f32_e32 v4, v4
	v_add_u32_e32 v5, s4, v1
	v_mul_f32_e32 v4, 0x4f7ffffe, v4
	v_cvt_u32_f32_e32 v4, v4
	v_mul_lo_u32 v1, v3, v4
	v_mul_hi_u32 v1, v4, v1
	v_add_u32_e32 v1, v4, v1
	v_mul_hi_u32 v1, v5, v1
	v_mul_lo_u32 v3, v1, v2
	v_sub_u32_e32 v3, v5, v3
	v_add_u32_e32 v4, 1, v1
	v_cmp_ge_u32_e32 vcc, v3, v2
	s_nop 1
	v_cndmask_b32_e32 v1, v1, v4, vcc
	v_sub_u32_e32 v4, v3, v2
	v_cndmask_b32_e32 v3, v3, v4, vcc
	v_add_u32_e32 v4, 1, v1
	v_cmp_ge_u32_e32 vcc, v3, v2
	v_add_u32_e32 v3, 1, v5
	s_nop 0
	v_cndmask_b32_e32 v1, v1, v4, vcc
	v_mul_lo_u32 v4, v2, v1
	v_add_u32_e32 v2, v4, v2
	v_cmp_ne_u32_e32 vcc, v3, v2
	s_and_saveexec_b64 s[4:5], vcc
	s_xor_b64 s[4:5], exec, s[4:5]
	s_cbranch_execz .LBB0_704
	s_waitcnt lgkmcnt(0)
	v_mov_b32_e32 v0, 0x2000
	global_load_dword v0, v0, s[2:3] offset:1024 sc1
	s_add_u32 s10, s2, 0x2400
	s_addc_u32 s11, s3, 0
	s_waitcnt vmcnt(0)
	v_cmp_eq_u32_e32 vcc, v0, v1
	s_and_saveexec_b64 s[6:7], vcc
	s_cbranch_execz .LBB0_703
	s_mov_b32 s18, 1
	s_mov_b64 s[12:13], 0
	v_mov_b32_e32 v0, 0
	s_branch .LBB0_694

.LBB0_760:
	s_or_b64 exec, exec, s[6:7]
	v_cvt_f32_u32_e32 v4, v2
	s_waitcnt vmcnt(1)
	v_readfirstlane_b32 s4, v3
	v_sub_u32_e32 v3, 0, v2
	v_rcp_iflag_f32_e32 v4, v4
	v_add_u32_e32 v5, s4, v1
	v_mul_f32_e32 v4, 0x4f7ffffe, v4
	v_cvt_u32_f32_e32 v4, v4
	v_mul_lo_u32 v1, v3, v4
	v_mul_hi_u32 v1, v4, v1
	v_add_u32_e32 v1, v4, v1
	v_mul_hi_u32 v1, v5, v1
	v_mul_lo_u32 v3, v1, v2
	v_sub_u32_e32 v3, v5, v3
	v_add_u32_e32 v4, 1, v1
	v_cmp_ge_u32_e32 vcc, v3, v2
	s_nop 1
	v_cndmask_b32_e32 v1, v1, v4, vcc
	v_sub_u32_e32 v4, v3, v2
	v_cndmask_b32_e32 v3, v3, v4, vcc
	v_add_u32_e32 v4, 1, v1
	v_cmp_ge_u32_e32 vcc, v3, v2
	v_add_u32_e32 v3, 1, v5
	s_nop 0
	v_cndmask_b32_e32 v1, v1, v4, vcc
	v_mul_lo_u32 v4, v2, v1
	v_add_u32_e32 v2, v4, v2
	v_cmp_ne_u32_e32 vcc, v3, v2
	s_and_saveexec_b64 s[4:5], vcc
	s_xor_b64 s[4:5], exec, s[4:5]
	s_cbranch_execz .LBB0_774
	s_waitcnt lgkmcnt(0)
	v_mov_b32_e32 v0, 0x2000
	global_load_dword v0, v0, s[2:3] offset:1024 sc1
	s_add_u32 s12, s2, 0x2400
	s_addc_u32 s13, s3, 0
	s_waitcnt vmcnt(0)
	v_cmp_eq_u32_e32 vcc, v0, v1
	s_and_saveexec_b64 s[6:7], vcc
	s_cbranch_execz .LBB0_773
	s_mov_b32 s18, 1
	s_mov_b64 s[14:15], 0
	v_mov_b32_e32 v0, 0
	s_branch .LBB0_764

.LBB0_856:
	s_mov_b64 s[4:5], exec
	v_readlane_b32 s2, v254, 38
	s_lshl_b32 s2, s2, 8
	v_mbcnt_lo_u32_b32 v1, s4, 0
	s_add_u32 s2, s72, s2
	v_mbcnt_hi_u32_b32 v1, s5, v1
	s_addc_u32 s3, s73, 0
	v_cmp_eq_u32_e32 vcc, 0, v1
	s_and_saveexec_b64 s[12:13], vcc
	s_cbranch_execz .LBB0_858
	s_bcnt1_i32_b64 s4, s[4:5]
	v_mov_b32_e32 v3, 0x1000
	v_mov_b32_e32 v4, s4
	global_atomic_add v3, v3, v4, s[2:3] offset:1024 sc0
	buffer_inv sc1
.LBB0_858:
	s_or_b64 exec, exec, s[12:13]
	v_cvt_f32_u32_e32 v4, v2
	s_waitcnt vmcnt(1)
	v_readfirstlane_b32 s4, v3
	v_sub_u32_e32 v3, 0, v2
	v_rcp_iflag_f32_e32 v4, v4
	v_add_u32_e32 v5, s4, v1
	v_mul_f32_e32 v4, 0x4f7ffffe, v4
	v_cvt_u32_f32_e32 v4, v4
	v_mul_lo_u32 v1, v3, v4
	v_mul_hi_u32 v1, v4, v1
	v_add_u32_e32 v1, v4, v1
	v_mul_hi_u32 v1, v5, v1
	v_mul_lo_u32 v3, v1, v2
	v_sub_u32_e32 v3, v5, v3
	v_add_u32_e32 v4, 1, v1
	v_cmp_ge_u32_e32 vcc, v3, v2
	s_nop 1
	v_cndmask_b32_e32 v1, v1, v4, vcc
	v_sub_u32_e32 v4, v3, v2
	v_cndmask_b32_e32 v3, v3, v4, vcc
	v_add_u32_e32 v4, 1, v1
	v_cmp_ge_u32_e32 vcc, v3, v2
	v_add_u32_e32 v3, 1, v5
	s_nop 0
	v_cndmask_b32_e32 v1, v1, v4, vcc
	v_mul_lo_u32 v4, v2, v1
	v_add_u32_e32 v2, v4, v2
	v_cmp_ne_u32_e32 vcc, v3, v2
	s_and_saveexec_b64 s[4:5], vcc
	s_xor_b64 s[4:5], exec, s[4:5]
	s_cbranch_execz .LBB0_872
	s_waitcnt lgkmcnt(0)
	v_mov_b32_e32 v0, 0x2000
	global_load_dword v0, v0, s[2:3] offset:1024 sc1
	s_add_u32 s14, s2, 0x2400
	s_addc_u32 s15, s3, 0
	s_waitcnt vmcnt(0)
	v_cmp_eq_u32_e32 vcc, v0, v1
	s_and_saveexec_b64 s[12:13], vcc
	s_cbranch_execz .LBB0_871
	s_mov_b32 s18, 1
	s_mov_b64 s[16:17], 0
	v_mov_b32_e32 v0, 0
	s_branch .LBB0_862

.LBB0_946:
	s_mov_b64 s[6:7], exec
	v_readlane_b32 s4, v254, 38
	s_lshl_b32 s4, s4, 8
	v_mbcnt_lo_u32_b32 v1, s6, 0
	s_add_u32 s4, s72, s4
	v_mbcnt_hi_u32_b32 v1, s7, v1
	s_addc_u32 s5, s73, 0
	v_cmp_eq_u32_e32 vcc, 0, v1
	s_and_saveexec_b64 s[12:13], vcc
	s_cbranch_execz .LBB0_948
	s_bcnt1_i32_b64 s6, s[6:7]
	v_mov_b32_e32 v3, 0x1000
	v_mov_b32_e32 v4, s6
	global_atomic_add v3, v3, v4, s[4:5] offset:1024 sc0
	buffer_inv sc1
.LBB0_948:
	s_or_b64 exec, exec, s[12:13]
	v_cvt_f32_u32_e32 v4, v2
	s_waitcnt vmcnt(1)
	v_readfirstlane_b32 s6, v3
	v_sub_u32_e32 v3, 0, v2
	v_rcp_iflag_f32_e32 v4, v4
	v_add_u32_e32 v5, s6, v1
	v_mul_f32_e32 v4, 0x4f7ffffe, v4
	v_cvt_u32_f32_e32 v4, v4
	v_mul_lo_u32 v1, v3, v4
	v_mul_hi_u32 v1, v4, v1
	v_add_u32_e32 v1, v4, v1
	v_mul_hi_u32 v1, v5, v1
	v_mul_lo_u32 v3, v1, v2
	v_sub_u32_e32 v3, v5, v3
	v_add_u32_e32 v4, 1, v1
	v_cmp_ge_u32_e32 vcc, v3, v2
	s_nop 1
	v_cndmask_b32_e32 v1, v1, v4, vcc
	v_sub_u32_e32 v4, v3, v2
	v_cndmask_b32_e32 v3, v3, v4, vcc
	v_add_u32_e32 v4, 1, v1
	v_cmp_ge_u32_e32 vcc, v3, v2
	v_add_u32_e32 v3, 1, v5
	s_nop 0
	v_cndmask_b32_e32 v1, v1, v4, vcc
	v_mul_lo_u32 v4, v2, v1
	v_add_u32_e32 v2, v4, v2
	v_cmp_ne_u32_e32 vcc, v3, v2
	s_and_saveexec_b64 s[6:7], vcc
	s_xor_b64 s[6:7], exec, s[6:7]
	s_cbranch_execz .LBB0_962
	s_waitcnt lgkmcnt(0)
	v_mov_b32_e32 v0, 0x2000
	global_load_dword v0, v0, s[4:5] offset:1024 sc1
	s_add_u32 s14, s4, 0x2400
	s_addc_u32 s15, s5, 0
	s_waitcnt vmcnt(0)
	v_cmp_eq_u32_e32 vcc, v0, v1
	s_and_saveexec_b64 s[12:13], vcc
	s_cbranch_execz .LBB0_961
	s_mov_b32 s18, 1
	s_mov_b64 s[16:17], 0
	v_mov_b32_e32 v0, 0
	s_branch .LBB0_952

.LBB0_1128:
	s_or_b64 exec, exec, s[6:7]
	v_cvt_f32_u32_e32 v4, v2
	s_waitcnt vmcnt(1)
	v_readfirstlane_b32 s4, v3
	v_sub_u32_e32 v3, 0, v2
	v_rcp_iflag_f32_e32 v4, v4
	v_add_u32_e32 v5, s4, v1
	v_mul_f32_e32 v4, 0x4f7ffffe, v4
	v_cvt_u32_f32_e32 v4, v4
	v_mul_lo_u32 v1, v3, v4
	v_mul_hi_u32 v1, v4, v1
	v_add_u32_e32 v1, v4, v1
	v_mul_hi_u32 v1, v5, v1
	v_mul_lo_u32 v3, v1, v2
	v_sub_u32_e32 v3, v5, v3
	v_add_u32_e32 v4, 1, v1
	v_cmp_ge_u32_e32 vcc, v3, v2
	s_nop 1
	v_cndmask_b32_e32 v1, v1, v4, vcc
	v_sub_u32_e32 v4, v3, v2
	v_cndmask_b32_e32 v3, v3, v4, vcc
	v_add_u32_e32 v4, 1, v1
	v_cmp_ge_u32_e32 vcc, v3, v2
	v_add_u32_e32 v3, 1, v5
	s_nop 0
	v_cndmask_b32_e32 v1, v1, v4, vcc
	v_mul_lo_u32 v4, v2, v1
	v_add_u32_e32 v2, v4, v2
	v_cmp_ne_u32_e32 vcc, v3, v2
	s_and_saveexec_b64 s[4:5], vcc
	s_xor_b64 s[4:5], exec, s[4:5]
	s_cbranch_execz .LBB0_1142
	s_waitcnt lgkmcnt(0)
	v_mov_b32_e32 v0, 0x2000
	global_load_dword v0, v0, s[2:3] offset:1024 sc1
	s_add_u32 s8, s2, 0x2400
	s_addc_u32 s9, s3, 0
	s_waitcnt vmcnt(0)
	v_cmp_eq_u32_e32 vcc, v0, v1
	s_and_saveexec_b64 s[6:7], vcc
	s_cbranch_execz .LBB0_1141
	s_mov_b32 s18, 1
	s_mov_b64 s[10:11], 0
	v_mov_b32_e32 v0, 0
	s_branch .LBB0_1132

.LBB0_1733:
	s_mov_b64 s[4:5], exec
	v_readlane_b32 s2, v254, 38
	s_lshl_b32 s2, s2, 8
	v_mbcnt_lo_u32_b32 v1, s4, 0
	s_add_u32 s2, s72, s2
	v_mbcnt_hi_u32_b32 v1, s5, v1
	s_addc_u32 s3, s73, 0
	v_cmp_eq_u32_e32 vcc, 0, v1
	s_and_saveexec_b64 s[8:9], vcc
	s_cbranch_execz .LBB0_1735
	s_bcnt1_i32_b64 s4, s[4:5]
	v_mov_b32_e32 v3, 0x1000
	v_mov_b32_e32 v4, s4
	global_atomic_add v3, v3, v4, s[2:3] offset:1024 sc0
	buffer_inv sc1
.LBB0_1735:
	s_or_b64 exec, exec, s[8:9]
	v_cvt_f32_u32_e32 v4, v2
	s_waitcnt vmcnt(1)
	v_readfirstlane_b32 s4, v3
	v_sub_u32_e32 v3, 0, v2
	v_rcp_iflag_f32_e32 v4, v4
	v_add_u32_e32 v5, s4, v1
	v_mul_f32_e32 v4, 0x4f7ffffe, v4
	v_cvt_u32_f32_e32 v4, v4
	v_mul_lo_u32 v1, v3, v4
	v_mul_hi_u32 v1, v4, v1
	v_add_u32_e32 v1, v4, v1
	v_mul_hi_u32 v1, v5, v1
	v_mul_lo_u32 v3, v1, v2
	v_sub_u32_e32 v3, v5, v3
	v_add_u32_e32 v4, 1, v1
	v_cmp_ge_u32_e32 vcc, v3, v2
	s_nop 1
	v_cndmask_b32_e32 v1, v1, v4, vcc
	v_sub_u32_e32 v4, v3, v2
	v_cndmask_b32_e32 v3, v3, v4, vcc
	v_add_u32_e32 v4, 1, v1
	v_cmp_ge_u32_e32 vcc, v3, v2
	v_add_u32_e32 v3, 1, v5
	s_nop 0
	v_cndmask_b32_e32 v1, v1, v4, vcc
	v_mul_lo_u32 v4, v2, v1
	v_add_u32_e32 v2, v4, v2
	v_cmp_ne_u32_e32 vcc, v3, v2
	s_and_saveexec_b64 s[4:5], vcc
	s_xor_b64 s[4:5], exec, s[4:5]
	s_cbranch_execz .LBB0_1749
	s_waitcnt lgkmcnt(0)
	v_mov_b32_e32 v0, 0x2000
	global_load_dword v0, v0, s[2:3] offset:1024 sc1
	s_add_u32 s10, s2, 0x2400
	s_addc_u32 s11, s3, 0
	s_waitcnt vmcnt(0)
	v_cmp_eq_u32_e32 vcc, v0, v1
	s_and_saveexec_b64 s[8:9], vcc
	s_cbranch_execz .LBB0_1748
	s_mov_b32 s18, 1
	s_mov_b64 s[12:13], 0
	v_mov_b32_e32 v0, 0
	s_branch .LBB0_1739

.LBB0_1823:
	s_mov_b64 s[6:7], exec
	v_readlane_b32 s4, v254, 38
	s_lshl_b32 s4, s4, 8
	v_mbcnt_lo_u32_b32 v1, s6, 0
	s_add_u32 s4, s72, s4
	v_mbcnt_hi_u32_b32 v1, s7, v1
	s_addc_u32 s5, s73, 0
	v_cmp_eq_u32_e32 vcc, 0, v1
	s_and_saveexec_b64 s[8:9], vcc
	s_cbranch_execz .LBB0_1825
	s_bcnt1_i32_b64 s6, s[6:7]
	v_mov_b32_e32 v3, 0x1000
	v_mov_b32_e32 v4, s6
	global_atomic_add v3, v3, v4, s[4:5] offset:1024 sc0
	buffer_inv sc1
.LBB0_1825:
	s_or_b64 exec, exec, s[8:9]
	v_cvt_f32_u32_e32 v4, v2
	s_waitcnt vmcnt(1)
	v_readfirstlane_b32 s6, v3
	v_sub_u32_e32 v3, 0, v2
	v_rcp_iflag_f32_e32 v4, v4
	v_add_u32_e32 v5, s6, v1
	v_mul_f32_e32 v4, 0x4f7ffffe, v4
	v_cvt_u32_f32_e32 v4, v4
	v_mul_lo_u32 v1, v3, v4
	v_mul_hi_u32 v1, v4, v1
	v_add_u32_e32 v1, v4, v1
	v_mul_hi_u32 v1, v5, v1
	v_mul_lo_u32 v3, v1, v2
	v_sub_u32_e32 v3, v5, v3
	v_add_u32_e32 v4, 1, v1
	v_cmp_ge_u32_e32 vcc, v3, v2
	s_nop 1
	v_cndmask_b32_e32 v1, v1, v4, vcc
	v_sub_u32_e32 v4, v3, v2
	v_cndmask_b32_e32 v3, v3, v4, vcc
	v_add_u32_e32 v4, 1, v1
	v_cmp_ge_u32_e32 vcc, v3, v2
	v_add_u32_e32 v3, 1, v5
	s_nop 0
	v_cndmask_b32_e32 v1, v1, v4, vcc
	v_mul_lo_u32 v4, v2, v1
	v_add_u32_e32 v2, v4, v2
	v_cmp_ne_u32_e32 vcc, v3, v2
	s_and_saveexec_b64 s[6:7], vcc
	s_xor_b64 s[6:7], exec, s[6:7]
	s_cbranch_execz .LBB0_1839
	s_waitcnt lgkmcnt(0)
	v_mov_b32_e32 v0, 0x2000
	global_load_dword v0, v0, s[4:5] offset:1024 sc1
	s_add_u32 s10, s4, 0x2400
	s_addc_u32 s11, s5, 0
	s_waitcnt vmcnt(0)
	v_cmp_eq_u32_e32 vcc, v0, v1
	s_and_saveexec_b64 s[8:9], vcc
	s_cbranch_execz .LBB0_1838
	s_mov_b32 s18, 1
	s_mov_b64 s[12:13], 0
	v_mov_b32_e32 v0, 0
	s_branch .LBB0_1829

.LBB0_2327:
	s_or_b64 exec, exec, s[6:7]
	v_cvt_f32_u32_e32 v4, v2
	s_waitcnt vmcnt(1)
	v_readfirstlane_b32 s4, v3
	v_sub_u32_e32 v3, 0, v2
	v_rcp_iflag_f32_e32 v4, v4
	v_add_u32_e32 v5, s4, v1
	v_mul_f32_e32 v4, 0x4f7ffffe, v4
	v_cvt_u32_f32_e32 v4, v4
	v_mul_lo_u32 v1, v3, v4
	v_mul_hi_u32 v1, v4, v1
	v_add_u32_e32 v1, v4, v1
	v_mul_hi_u32 v1, v5, v1
	v_mul_lo_u32 v3, v1, v2
	v_sub_u32_e32 v3, v5, v3
	v_add_u32_e32 v4, 1, v1
	v_cmp_ge_u32_e32 vcc, v3, v2
	s_nop 1
	v_cndmask_b32_e32 v1, v1, v4, vcc
	v_sub_u32_e32 v4, v3, v2
	v_cndmask_b32_e32 v3, v3, v4, vcc
	v_add_u32_e32 v4, 1, v1
	v_cmp_ge_u32_e32 vcc, v3, v2
	v_add_u32_e32 v3, 1, v5
	s_nop 0
	v_cndmask_b32_e32 v1, v1, v4, vcc
	v_mul_lo_u32 v4, v2, v1
	v_add_u32_e32 v2, v4, v2
	v_cmp_ne_u32_e32 vcc, v3, v2
	s_and_saveexec_b64 s[4:5], vcc
	s_xor_b64 s[4:5], exec, s[4:5]
	s_cbranch_execz .LBB0_2341
	s_waitcnt lgkmcnt(0)
	v_mov_b32_e32 v0, 0x2000
	global_load_dword v0, v0, s[2:3] offset:1024 sc1
	s_add_u32 s8, s2, 0x2400
	s_addc_u32 s9, s3, 0
	s_waitcnt vmcnt(0)
	v_cmp_eq_u32_e32 vcc, v0, v1
	s_and_saveexec_b64 s[6:7], vcc
	s_cbranch_execz .LBB0_2340
	s_mov_b32 s20, 1
	s_mov_b64 s[10:11], 0
	v_mov_b32_e32 v0, 0
	s_branch .LBB0_2331

.LBB0_2446:
	s_or_b64 exec, exec, s[6:7]
	v_cvt_f32_u32_e32 v4, v2
	s_waitcnt vmcnt(1)
	v_readfirstlane_b32 s4, v3
	v_sub_u32_e32 v3, 0, v2
	v_rcp_iflag_f32_e32 v4, v4
	v_add_u32_e32 v5, s4, v1
	v_mul_f32_e32 v4, 0x4f7ffffe, v4
	v_cvt_u32_f32_e32 v4, v4
	v_mul_lo_u32 v1, v3, v4
	v_mul_hi_u32 v1, v4, v1
	v_add_u32_e32 v1, v4, v1
	v_mul_hi_u32 v1, v5, v1
	v_mul_lo_u32 v3, v1, v2
	v_sub_u32_e32 v3, v5, v3
	v_add_u32_e32 v4, 1, v1
	v_cmp_ge_u32_e32 vcc, v3, v2
	s_nop 1
	v_cndmask_b32_e32 v1, v1, v4, vcc
	v_sub_u32_e32 v4, v3, v2
	v_cndmask_b32_e32 v3, v3, v4, vcc
	v_add_u32_e32 v4, 1, v1
	v_cmp_ge_u32_e32 vcc, v3, v2
	v_add_u32_e32 v3, 1, v5
	s_nop 0
	v_cndmask_b32_e32 v1, v1, v4, vcc
	v_mul_lo_u32 v4, v2, v1
	v_add_u32_e32 v2, v4, v2
	v_cmp_ne_u32_e32 vcc, v3, v2
	s_and_saveexec_b64 s[4:5], vcc
	s_xor_b64 s[4:5], exec, s[4:5]
	s_cbranch_execz .LBB0_2460
	s_waitcnt lgkmcnt(0)
	v_mov_b32_e32 v0, 0x2000
	global_load_dword v0, v0, s[2:3] offset:1024 sc1
	s_add_u32 s8, s2, 0x2400
	s_addc_u32 s9, s3, 0
	s_waitcnt vmcnt(0)
	v_cmp_eq_u32_e32 vcc, v0, v1
	s_and_saveexec_b64 s[6:7], vcc
	s_cbranch_execz .LBB0_2459
	s_mov_b32 s24, 1
	s_mov_b64 s[10:11], 0
	v_mov_b32_e32 v0, 0
	s_branch .LBB0_2450

.LBB0_2516:
	s_or_b64 exec, exec, s[6:7]
	v_cvt_f32_u32_e32 v4, v2
	s_waitcnt vmcnt(1)
	v_readfirstlane_b32 s4, v3
	v_sub_u32_e32 v3, 0, v2
	v_rcp_iflag_f32_e32 v4, v4
	v_add_u32_e32 v5, s4, v1
	v_mul_f32_e32 v4, 0x4f7ffffe, v4
	v_cvt_u32_f32_e32 v4, v4
	v_mul_lo_u32 v1, v3, v4
	v_mul_hi_u32 v1, v4, v1
	v_add_u32_e32 v1, v4, v1
	v_mul_hi_u32 v1, v5, v1
	v_mul_lo_u32 v3, v1, v2
	v_sub_u32_e32 v3, v5, v3
	v_add_u32_e32 v4, 1, v1
	v_cmp_ge_u32_e32 vcc, v3, v2
	s_nop 1
	v_cndmask_b32_e32 v1, v1, v4, vcc
	v_sub_u32_e32 v4, v3, v2
	v_cndmask_b32_e32 v3, v3, v4, vcc
	v_add_u32_e32 v4, 1, v1
	v_cmp_ge_u32_e32 vcc, v3, v2
	v_add_u32_e32 v3, 1, v5
	s_nop 0
	v_cndmask_b32_e32 v1, v1, v4, vcc
	v_mul_lo_u32 v4, v2, v1
	v_add_u32_e32 v2, v4, v2
	v_cmp_ne_u32_e32 vcc, v3, v2
	s_and_saveexec_b64 s[4:5], vcc
	s_xor_b64 s[4:5], exec, s[4:5]
	s_cbranch_execz .LBB0_2530
	s_waitcnt lgkmcnt(0)
	v_mov_b32_e32 v0, 0x2000
	global_load_dword v0, v0, s[2:3] offset:1024 sc1
	s_add_u32 s8, s2, 0x2400
	s_addc_u32 s9, s3, 0
	s_waitcnt vmcnt(0)
	v_cmp_eq_u32_e32 vcc, v0, v1
	s_and_saveexec_b64 s[6:7], vcc
	s_cbranch_execz .LBB0_2529
	s_mov_b32 s26, 1
	s_mov_b64 s[10:11], 0
	v_mov_b32_e32 v0, 0
	s_branch .LBB0_2520

.LBB0_2614:
	s_or_b64 exec, exec, s[8:9]
	v_cvt_f32_u32_e32 v4, v2
	s_waitcnt vmcnt(1)
	v_readfirstlane_b32 s4, v3
	v_sub_u32_e32 v3, 0, v2
	v_rcp_iflag_f32_e32 v4, v4
	v_add_u32_e32 v5, s4, v1
	v_mul_f32_e32 v4, 0x4f7ffffe, v4
	v_cvt_u32_f32_e32 v4, v4
	v_mul_lo_u32 v1, v3, v4
	v_mul_hi_u32 v1, v4, v1
	v_add_u32_e32 v1, v4, v1
	v_mul_hi_u32 v1, v5, v1
	v_mul_lo_u32 v3, v1, v2
	v_sub_u32_e32 v3, v5, v3
	v_add_u32_e32 v4, 1, v1
	v_cmp_ge_u32_e32 vcc, v3, v2
	s_nop 1
	v_cndmask_b32_e32 v1, v1, v4, vcc
	v_sub_u32_e32 v4, v3, v2
	v_cndmask_b32_e32 v3, v3, v4, vcc
	v_add_u32_e32 v4, 1, v1
	v_cmp_ge_u32_e32 vcc, v3, v2
	v_add_u32_e32 v3, 1, v5
	s_nop 0
	v_cndmask_b32_e32 v1, v1, v4, vcc
	v_mul_lo_u32 v4, v2, v1
	v_add_u32_e32 v2, v4, v2
	v_cmp_ne_u32_e32 vcc, v3, v2
	s_and_saveexec_b64 s[4:5], vcc
	s_xor_b64 s[4:5], exec, s[4:5]
	s_cbranch_execz .LBB0_2628
	s_waitcnt lgkmcnt(0)
	v_mov_b32_e32 v0, 0x2000
	global_load_dword v0, v0, s[2:3] offset:1024 sc1
	s_add_u32 s10, s2, 0x2400
	s_addc_u32 s11, s3, 0
	s_waitcnt vmcnt(0)
	v_cmp_eq_u32_e32 vcc, v0, v1
	s_and_saveexec_b64 s[8:9], vcc
	s_cbranch_execz .LBB0_2627
	s_mov_b32 s28, 1
	s_mov_b64 s[12:13], 0
	v_mov_b32_e32 v0, 0
	s_branch .LBB0_2618

.LBB0_2704:
	s_or_b64 exec, exec, s[8:9]
	v_cvt_f32_u32_e32 v4, v2
	s_waitcnt vmcnt(1)
	v_readfirstlane_b32 s6, v3
	v_sub_u32_e32 v3, 0, v2
	v_rcp_iflag_f32_e32 v4, v4
	v_add_u32_e32 v5, s6, v1
	v_mul_f32_e32 v4, 0x4f7ffffe, v4
	v_cvt_u32_f32_e32 v4, v4
	v_mul_lo_u32 v1, v3, v4
	v_mul_hi_u32 v1, v4, v1
	v_add_u32_e32 v1, v4, v1
	v_mul_hi_u32 v1, v5, v1
	v_mul_lo_u32 v3, v1, v2
	v_sub_u32_e32 v3, v5, v3
	v_add_u32_e32 v4, 1, v1
	v_cmp_ge_u32_e32 vcc, v3, v2
	s_nop 1
	v_cndmask_b32_e32 v1, v1, v4, vcc
	v_sub_u32_e32 v4, v3, v2
	v_cndmask_b32_e32 v3, v3, v4, vcc
	v_add_u32_e32 v4, 1, v1
	v_cmp_ge_u32_e32 vcc, v3, v2
	v_add_u32_e32 v3, 1, v5
	s_nop 0
	v_cndmask_b32_e32 v1, v1, v4, vcc
	v_mul_lo_u32 v4, v2, v1
	v_add_u32_e32 v2, v4, v2
	v_cmp_ne_u32_e32 vcc, v3, v2
	s_and_saveexec_b64 s[6:7], vcc
	s_xor_b64 s[6:7], exec, s[6:7]
	s_cbranch_execz .LBB0_2718
	s_waitcnt lgkmcnt(0)
	v_mov_b32_e32 v0, 0x2000
	global_load_dword v0, v0, s[4:5] offset:1024 sc1
	s_add_u32 s10, s4, 0x2400
	s_addc_u32 s11, s5, 0
	s_waitcnt vmcnt(0)
	v_cmp_eq_u32_e32 vcc, v0, v1
	s_and_saveexec_b64 s[8:9], vcc
	s_cbranch_execz .LBB0_2717
	s_mov_b32 s28, 1
	s_mov_b64 s[12:13], 0
	v_mov_b32_e32 v0, 0
	s_branch .LBB0_2708

.LBB0_2962:
	s_or_b64 exec, exec, s[8:9]
	v_cvt_f32_u32_e32 v4, v2
	s_waitcnt vmcnt(1)
	v_readfirstlane_b32 s6, v3
	v_sub_u32_e32 v3, 0, v2
	v_rcp_iflag_f32_e32 v4, v4
	v_add_u32_e32 v5, s6, v1
	v_mul_f32_e32 v4, 0x4f7ffffe, v4
	v_cvt_u32_f32_e32 v4, v4
	v_mul_lo_u32 v1, v3, v4
	v_mul_hi_u32 v1, v4, v1
	v_add_u32_e32 v1, v4, v1
	v_mul_hi_u32 v1, v5, v1
	v_mul_lo_u32 v3, v1, v2
	v_sub_u32_e32 v3, v5, v3
	v_add_u32_e32 v4, 1, v1
	v_cmp_ge_u32_e32 vcc, v3, v2
	s_nop 1
	v_cndmask_b32_e32 v1, v1, v4, vcc
	v_sub_u32_e32 v4, v3, v2
	v_cndmask_b32_e32 v3, v3, v4, vcc
	v_add_u32_e32 v4, 1, v1
	v_cmp_ge_u32_e32 vcc, v3, v2
	v_add_u32_e32 v3, 1, v5
	s_nop 0
	v_cndmask_b32_e32 v1, v1, v4, vcc
	v_mul_lo_u32 v4, v2, v1
	v_add_u32_e32 v2, v4, v2
	v_cmp_ne_u32_e32 vcc, v3, v2
	s_and_saveexec_b64 s[6:7], vcc
	s_xor_b64 s[6:7], exec, s[6:7]
	s_cbranch_execz .LBB0_2976
	s_waitcnt lgkmcnt(0)
	v_mov_b32_e32 v0, 0x2000
	global_load_dword v0, v0, s[4:5] offset:1024 sc1
	s_add_u32 s10, s4, 0x2400
	s_addc_u32 s11, s5, 0
	s_waitcnt vmcnt(0)
	v_cmp_eq_u32_e32 vcc, v0, v1
	s_and_saveexec_b64 s[8:9], vcc
	s_cbranch_execz .LBB0_2975
	s_mov_b32 s22, 1
	s_mov_b64 s[12:13], 0
	v_mov_b32_e32 v0, 0
	s_branch .LBB0_2966

.LBB0_3194:
	s_or_b64 exec, exec, s[6:7]
	v_cvt_f32_u32_e32 v4, v2
	s_waitcnt vmcnt(1)
	v_readfirstlane_b32 s4, v3
	v_sub_u32_e32 v3, 0, v2
	v_rcp_iflag_f32_e32 v4, v4
	v_add_u32_e32 v5, s4, v1
	v_mul_f32_e32 v4, 0x4f7ffffe, v4
	v_cvt_u32_f32_e32 v4, v4
	v_mul_lo_u32 v1, v3, v4
	v_mul_hi_u32 v1, v4, v1
	v_add_u32_e32 v1, v4, v1
	v_mul_hi_u32 v1, v5, v1
	v_mul_lo_u32 v3, v1, v2
	v_sub_u32_e32 v3, v5, v3
	v_add_u32_e32 v4, 1, v1
	v_cmp_ge_u32_e32 vcc, v3, v2
	s_nop 1
	v_cndmask_b32_e32 v1, v1, v4, vcc
	v_sub_u32_e32 v4, v3, v2
	v_cndmask_b32_e32 v3, v3, v4, vcc
	v_add_u32_e32 v4, 1, v1
	v_cmp_ge_u32_e32 vcc, v3, v2
	v_add_u32_e32 v3, 1, v5
	s_nop 0
	v_cndmask_b32_e32 v1, v1, v4, vcc
	v_mul_lo_u32 v4, v2, v1
	v_add_u32_e32 v2, v4, v2
	v_cmp_ne_u32_e32 vcc, v3, v2
	s_and_saveexec_b64 s[4:5], vcc
	s_xor_b64 s[4:5], exec, s[4:5]
	s_cbranch_execz .LBB0_3208
	s_waitcnt lgkmcnt(0)
	v_mov_b32_e32 v0, 0x2000
	global_load_dword v0, v0, s[2:3] offset:1024 sc1
	s_add_u32 s10, s2, 0x2400
	s_addc_u32 s11, s3, 0
	s_waitcnt vmcnt(0)
	v_cmp_eq_u32_e32 vcc, v0, v1
	s_and_saveexec_b64 s[6:7], vcc
	s_cbranch_execz .LBB0_3207
	s_mov_b32 s24, 1
	s_mov_b64 s[12:13], 0
	v_mov_b32_e32 v0, 0
	s_branch .LBB0_3198

.LBB0_3362:
	s_or_b64 exec, exec, s[8:9]
	v_cvt_f32_u32_e32 v4, v2
	s_waitcnt vmcnt(1)
	v_readfirstlane_b32 s4, v3
	v_sub_u32_e32 v3, 0, v2
	v_rcp_iflag_f32_e32 v4, v4
	v_add_u32_e32 v5, s4, v1
	v_mul_f32_e32 v4, 0x4f7ffffe, v4
	v_cvt_u32_f32_e32 v4, v4
	v_mul_lo_u32 v1, v3, v4
	v_mul_hi_u32 v1, v4, v1
	v_add_u32_e32 v1, v4, v1
	v_mul_hi_u32 v1, v5, v1
	v_mul_lo_u32 v3, v1, v2
	v_sub_u32_e32 v3, v5, v3
	v_add_u32_e32 v4, 1, v1
	v_cmp_ge_u32_e32 vcc, v3, v2
	s_nop 1
	v_cndmask_b32_e32 v1, v1, v4, vcc
	v_sub_u32_e32 v4, v3, v2
	v_cndmask_b32_e32 v3, v3, v4, vcc
	v_add_u32_e32 v4, 1, v1
	v_cmp_ge_u32_e32 vcc, v3, v2
	v_add_u32_e32 v3, 1, v5
	s_nop 0
	v_cndmask_b32_e32 v1, v1, v4, vcc
	v_mul_lo_u32 v4, v2, v1
	v_add_u32_e32 v2, v4, v2
	v_cmp_ne_u32_e32 vcc, v3, v2
	s_and_saveexec_b64 s[4:5], vcc
	s_xor_b64 s[4:5], exec, s[4:5]
	s_cbranch_execz .LBB0_3376
	s_waitcnt lgkmcnt(0)
	v_mov_b32_e32 v0, 0x2000
	global_load_dword v0, v0, s[2:3] offset:1024 sc1
	s_add_u32 s10, s2, 0x2400
	s_addc_u32 s11, s3, 0
	s_waitcnt vmcnt(0)
	v_cmp_eq_u32_e32 vcc, v0, v1
	s_and_saveexec_b64 s[8:9], vcc
	s_cbranch_execz .LBB0_3375
	s_mov_b32 s26, 1
	s_mov_b64 s[12:13], 0
	v_mov_b32_e32 v0, 0
	s_branch .LBB0_3366

.LBB0_3452:
	s_or_b64 exec, exec, s[8:9]
	v_cvt_f32_u32_e32 v4, v2
	s_waitcnt vmcnt(1)
	v_readfirstlane_b32 s6, v3
	v_sub_u32_e32 v3, 0, v2
	v_rcp_iflag_f32_e32 v4, v4
	v_add_u32_e32 v5, s6, v1
	v_mul_f32_e32 v4, 0x4f7ffffe, v4
	v_cvt_u32_f32_e32 v4, v4
	v_mul_lo_u32 v1, v3, v4
	v_mul_hi_u32 v1, v4, v1
	v_add_u32_e32 v1, v4, v1
	v_mul_hi_u32 v1, v5, v1
	v_mul_lo_u32 v3, v1, v2
	v_sub_u32_e32 v3, v5, v3
	v_add_u32_e32 v4, 1, v1
	v_cmp_ge_u32_e32 vcc, v3, v2
	s_nop 1
	v_cndmask_b32_e32 v1, v1, v4, vcc
	v_sub_u32_e32 v4, v3, v2
	v_cndmask_b32_e32 v3, v3, v4, vcc
	v_add_u32_e32 v4, 1, v1
	v_cmp_ge_u32_e32 vcc, v3, v2
	v_add_u32_e32 v3, 1, v5
	s_nop 0
	v_cndmask_b32_e32 v1, v1, v4, vcc
	v_mul_lo_u32 v4, v2, v1
	v_add_u32_e32 v2, v4, v2
	v_cmp_ne_u32_e32 vcc, v3, v2
	s_and_saveexec_b64 s[6:7], vcc
	s_xor_b64 s[6:7], exec, s[6:7]
	s_cbranch_execz .LBB0_3466
	s_waitcnt lgkmcnt(0)
	v_mov_b32_e32 v0, 0x2000
	global_load_dword v0, v0, s[4:5] offset:1024 sc1
	s_add_u32 s10, s4, 0x2400
	s_addc_u32 s11, s5, 0
	s_waitcnt vmcnt(0)
	v_cmp_eq_u32_e32 vcc, v0, v1
	s_and_saveexec_b64 s[8:9], vcc
	s_cbranch_execz .LBB0_3465
	s_mov_b32 s26, 1
	s_mov_b64 s[12:13], 0
	v_mov_b32_e32 v0, 0
	s_branch .LBB0_3456
